# plus merged dual GEMM final epilogue: x16 output scale applied to the accumulators while the gate loads are in flight (64 packed multiplies leave the post-wait path)
# speedup vs baseline: 1.0011x; 1.0011x over previous
.LBB0_445:
	v_lshl_add_u64 v[50:51], v[218:219], 0, s[58:59]
	global_load_dwordx4 v[188:191], v[50:51], off nt
	v_lshl_add_u64 v[50:51], v[218:219], 0, s[60:61]
	global_load_dwordx4 v[202:205], v[50:51], off nt
	v_lshl_add_u64 v[50:51], v[218:219], 0, s[62:63]
	global_load_dwordx4 v[184:187], v[50:51], off nt
	v_lshl_add_u64 v[50:51], v[218:219], 0, s[70:71]
	global_load_dwordx4 v[180:183], v[50:51], off nt
	v_lshl_add_u64 v[50:51], v[218:219], 0, s[78:79]
	global_load_dwordx4 v[176:179], v[50:51], off nt
	v_lshl_add_u64 v[50:51], v[218:219], 0, s[76:77]
	global_load_dwordx4 v[172:175], v[50:51], off nt
	v_lshl_add_u64 v[50:51], v[218:219], 0, s[74:75]
	global_load_dwordx4 v[168:171], v[50:51], off nt
	v_lshl_add_u64 v[50:51], v[218:219], 0, s[72:73]
	global_load_dwordx4 v[164:167], v[50:51], off nt
	v_lshl_add_u64 v[50:51], v[218:219], 0, s[68:69]
	s_or_b32 s0, s4, s7
	global_load_dwordx4 v[160:163], v[50:51], off nt
	v_lshl_add_u64 v[50:51], v[218:219], 0, s[66:67]
	s_ashr_i32 s1, s0, 31
	global_load_dwordx4 v[156:159], v[50:51], off nt
	v_lshl_add_u64 v[50:51], v[218:219], 0, s[64:65]
	s_lshl_b64 s[0:1], s[0:1], 10
	global_load_dwordx4 v[148:151], v[50:51], off nt
	v_lshl_add_u64 v[50:51], v[218:219], 0, s[0:1]
	s_or_b32 s0, s5, s40
	s_ashr_i32 s1, s0, 31
	s_lshl_b64 s[0:1], s[0:1], 10
	global_load_dwordx4 v[152:155], v[50:51], off nt
	v_lshl_add_u64 v[50:51], v[218:219], 0, s[0:1]
	s_or_b32 s0, s4, s40
	s_ashr_i32 s1, s0, 31
	s_lshl_b64 s[0:1], s[0:1], 10
	global_load_dwordx4 v[140:143], v[50:51], off nt
	v_lshl_add_u64 v[50:51], v[218:219], 0, s[0:1]
	s_or_b32 s0, s5, s41
	s_ashr_i32 s1, s0, 31
	s_lshl_b64 s[0:1], s[0:1], 10
	global_load_dwordx4 v[144:147], v[50:51], off nt
	v_lshl_add_u64 v[50:51], v[218:219], 0, s[0:1]
	s_or_b32 s0, s4, s41
	s_ashr_i32 s1, s0, 31
	s_lshl_b64 s[0:1], s[0:1], 10
	global_load_dwordx4 v[132:135], v[50:51], off nt
	v_lshl_add_u64 v[50:51], v[218:219], 0, s[0:1]
	global_load_dwordx4 v[136:139], v[50:51], off nt
	v_lshl_add_u32 v222, s36, 8, v199
	v_ashrrev_i32_e32 v223, 31, v222
	s_lshl_b32 vcc_lo, s20, 8
	s_ashr_i32 vcc_hi, vcc_lo, 31
	s_mov_b64 s[0:1], 0x20000
	v_pk_mul_f32 v[128:129], v[128:129], s[26:27] op_sel_hi:[1,0]
	v_pk_mul_f32 v[130:131], v[130:131], s[26:27] op_sel_hi:[1,0]
	v_pk_mul_f32 v[120:121], v[120:121], s[26:27] op_sel_hi:[1,0]
	v_pk_mul_f32 v[64:65], v[64:65], s[26:27] op_sel_hi:[1,0]
	v_pk_mul_f32 v[66:67], v[66:67], s[26:27] op_sel_hi:[1,0]
	v_pk_mul_f32 v[60:61], v[60:61], s[26:27] op_sel_hi:[1,0]
	v_pk_mul_f32 v[62:63], v[62:63], s[26:27] op_sel_hi:[1,0]
	v_pk_mul_f32 v[112:113], v[112:113], s[26:27] op_sel_hi:[1,0]
	v_pk_mul_f32 v[114:115], v[114:115], s[26:27] op_sel_hi:[1,0]
	v_pk_mul_f32 v[104:105], v[104:105], s[26:27] op_sel_hi:[1,0]
	v_pk_mul_f32 v[122:123], v[122:123], s[26:27] op_sel_hi:[1,0]
	v_pk_mul_f32 v[106:107], v[106:107], s[26:27] op_sel_hi:[1,0]
	v_pk_mul_f32 v[56:57], v[56:57], s[26:27] op_sel_hi:[1,0]
	v_pk_mul_f32 v[58:59], v[58:59], s[26:27] op_sel_hi:[1,0]
	v_pk_mul_f32 v[52:53], v[52:53], s[26:27] op_sel_hi:[1,0]
	v_pk_mul_f32 v[54:55], v[54:55], s[26:27] op_sel_hi:[1,0]
	v_pk_mul_f32 v[96:97], v[96:97], s[26:27] op_sel_hi:[1,0]
	v_pk_mul_f32 v[98:99], v[98:99], s[26:27] op_sel_hi:[1,0]
	v_pk_mul_f32 v[88:89], v[88:89], s[26:27] op_sel_hi:[1,0]
	v_pk_mul_f32 v[90:91], v[90:91], s[26:27] op_sel_hi:[1,0]
	v_pk_mul_f32 v[44:45], v[44:45], s[26:27] op_sel_hi:[1,0]
	v_pk_mul_f32 v[46:47], v[46:47], s[26:27] op_sel_hi:[1,0]
	v_pk_mul_f32 v[40:41], v[40:41], s[26:27] op_sel_hi:[1,0]
	v_pk_mul_f32 v[42:43], v[42:43], s[26:27] op_sel_hi:[1,0]
	v_pk_mul_f32 v[80:81], v[80:81], s[26:27] op_sel_hi:[1,0]
	v_pk_mul_f32 v[82:83], v[82:83], s[26:27] op_sel_hi:[1,0]
	v_pk_mul_f32 v[72:73], v[72:73], s[26:27] op_sel_hi:[1,0]
	v_pk_mul_f32 v[74:75], v[74:75], s[26:27] op_sel_hi:[1,0]
	v_pk_mul_f32 v[36:37], v[36:37], s[26:27] op_sel_hi:[1,0]
	v_pk_mul_f32 v[38:39], v[38:39], s[26:27] op_sel_hi:[1,0]
	v_pk_mul_f32 v[32:33], v[32:33], s[26:27] op_sel_hi:[1,0]
	v_pk_mul_f32 v[34:35], v[34:35], s[26:27] op_sel_hi:[1,0]
	v_pk_mul_f32 v[28:29], v[28:29], s[26:27] op_sel_hi:[1,0]
	v_pk_mul_f32 v[30:31], v[30:31], s[26:27] op_sel_hi:[1,0]
	v_pk_mul_f32 v[24:25], v[24:25], s[26:27] op_sel_hi:[1,0]
	v_pk_mul_f32 v[26:27], v[26:27], s[26:27] op_sel_hi:[1,0]
	v_pk_mul_f32 v[68:69], v[68:69], s[26:27] op_sel_hi:[1,0]
	v_pk_mul_f32 v[70:71], v[70:71], s[26:27] op_sel_hi:[1,0]
	v_pk_mul_f32 v[76:77], v[76:77], s[26:27] op_sel_hi:[1,0]
	v_pk_mul_f32 v[78:79], v[78:79], s[26:27] op_sel_hi:[1,0]
	v_pk_mul_f32 v[20:21], v[20:21], s[26:27] op_sel_hi:[1,0]
	v_pk_mul_f32 v[22:23], v[22:23], s[26:27] op_sel_hi:[1,0]
	v_pk_mul_f32 v[16:17], v[16:17], s[26:27] op_sel_hi:[1,0]
	v_pk_mul_f32 v[18:19], v[18:19], s[26:27] op_sel_hi:[1,0]
	v_pk_mul_f32 v[84:85], v[84:85], s[26:27] op_sel_hi:[1,0]
	v_pk_mul_f32 v[86:87], v[86:87], s[26:27] op_sel_hi:[1,0]
	v_pk_mul_f32 v[92:93], v[92:93], s[26:27] op_sel_hi:[1,0]
	v_pk_mul_f32 v[94:95], v[94:95], s[26:27] op_sel_hi:[1,0]
	v_pk_mul_f32 v[12:13], v[12:13], s[26:27] op_sel_hi:[1,0]
	v_pk_mul_f32 v[14:15], v[14:15], s[26:27] op_sel_hi:[1,0]
	v_pk_mul_f32 v[8:9], v[8:9], s[26:27] op_sel_hi:[1,0]
	v_pk_mul_f32 v[10:11], v[10:11], s[26:27] op_sel_hi:[1,0]
	v_pk_mul_f32 v[100:101], v[100:101], s[26:27] op_sel_hi:[1,0]
	v_pk_mul_f32 v[102:103], v[102:103], s[26:27] op_sel_hi:[1,0]
	v_pk_mul_f32 v[108:109], v[108:109], s[26:27] op_sel_hi:[1,0]
	v_pk_mul_f32 v[110:111], v[110:111], s[26:27] op_sel_hi:[1,0]
	v_pk_mul_f32 v[4:5], v[4:5], s[26:27] op_sel_hi:[1,0]
	v_pk_mul_f32 v[6:7], v[6:7], s[26:27] op_sel_hi:[1,0]
	v_pk_mul_f32 v[0:1], v[0:1], s[26:27] op_sel_hi:[1,0]
	v_pk_mul_f32 v[2:3], v[2:3], s[26:27] op_sel_hi:[1,0]
	v_pk_mul_f32 v[116:117], v[116:117], s[26:27] op_sel_hi:[1,0]
	v_pk_mul_f32 v[118:119], v[118:119], s[26:27] op_sel_hi:[1,0]
	v_pk_mul_f32 v[124:125], v[124:125], s[26:27] op_sel_hi:[1,0]
	v_pk_mul_f32 v[126:127], v[126:127], s[26:27] op_sel_hi:[1,0]
	s_waitcnt vmcnt(0)
	v_lshlrev_b32_e32 v224, 16, v188
	v_and_b32_e32 v225, 0xffff0000, v188
	v_lshlrev_b32_e32 v188, 16, v189
	v_and_b32_e32 v189, 0xffff0000, v189
	v_lshlrev_b32_e32 v194, 16, v202
	v_and_b32_e32 v195, 0xffff0000, v202
	v_lshlrev_b32_e32 v192, 16, v203
	v_and_b32_e32 v193, 0xffff0000, v203
	v_pk_mul_f32 v[202:203], v[128:129], v[224:225]
	v_pk_mul_f32 v[188:189], v[130:131], v[188:189]
	v_med3_f32 v48, v202, s11, v232
	v_med3_f32 v202, v203, s11, v232
	v_med3_f32 v203, v188, s11, v232
	v_mov_b32_e32 v188, v49
	v_cvt_pk_fp8_f32 v188, v48, v202
	v_lshlrev_b32_e32 v226, 16, v190
	v_and_b32_e32 v227, 0xffff0000, v190
	v_med3_f32 v189, v189, s11, v232
	v_cvt_pk_fp8_f32 v188, v203, v189 op_sel:[0,0,1]
	v_pk_mul_f32 v[202:203], v[120:121], v[226:227]
	v_pk_mul_f32 v[194:195], v[64:65], v[194:195]
	v_pk_mul_f32 v[192:193], v[66:67], v[192:193]
	v_med3_f32 v48, v202, s11, v232
	v_med3_f32 v202, v203, s11, v232
	v_mov_b32_e32 v189, v49
	v_cvt_pk_fp8_f32 v189, v48, v202
	v_med3_f32 v48, v194, s11, v232
	v_med3_f32 v194, v195, s11, v232
	v_med3_f32 v195, v192, s11, v232
	v_mov_b32_e32 v192, v49
	v_cvt_pk_fp8_f32 v192, v48, v194
	v_lshlrev_b32_e32 v234, 16, v191
	v_and_b32_e32 v235, 0xffff0000, v191
	v_lshlrev_b32_e32 v190, 16, v204
	v_and_b32_e32 v191, 0xffff0000, v204
	v_pk_mul_f32 v[190:191], v[60:61], v[190:191]
	v_med3_f32 v193, v193, s11, v232
	v_cvt_pk_fp8_f32 v192, v195, v193 op_sel:[0,0,1]
	v_med3_f32 v48, v190, s11, v232
	v_med3_f32 v190, v191, s11, v232
	v_mov_b32_e32 v193, v49
	v_lshlrev_b32_e32 v50, 16, v205
	v_and_b32_e32 v51, 0xffff0000, v205
	v_cvt_pk_fp8_f32 v193, v48, v190
	v_pk_mul_f32 v[50:51], v[62:63], v[50:51]
	v_mov_b32_e32 v190, v49
	v_lshlrev_b32_e32 v194, 16, v186
	v_med3_f32 v50, v50, s11, v232
	v_med3_f32 v51, v51, s11, v232
	v_cvt_pk_fp8_f32 v193, v50, v51 op_sel:[0,0,1]
	v_lshlrev_b32_e32 v50, 16, v184
	v_and_b32_e32 v51, 0xffff0000, v184
	v_pk_mul_f32 v[50:51], v[112:113], v[50:51]
	v_lshlrev_b32_e32 v184, 16, v185
	v_and_b32_e32 v185, 0xffff0000, v185
	v_med3_f32 v48, v50, s11, v232
	v_med3_f32 v50, v51, s11, v232
	v_cvt_pk_fp8_f32 v190, v48, v50
	v_pk_mul_f32 v[184:185], v[114:115], v[184:185]
	v_and_b32_e32 v195, 0xffff0000, v186
	v_mov_b32_e32 v191, v49
	v_med3_f32 v51, v184, s11, v232
	v_med3_f32 v184, v185, s11, v232
	v_cvt_pk_fp8_f32 v190, v51, v184 op_sel:[0,0,1]
	v_pk_mul_f32 v[50:51], v[104:105], v[194:195]
	v_pk_mul_f32 v[204:205], v[122:123], v[234:235]
	v_lshlrev_b32_e32 v186, 16, v187
	v_med3_f32 v48, v50, s11, v232
	v_med3_f32 v50, v51, s11, v232
	v_and_b32_e32 v187, 0xffff0000, v187
	v_cvt_pk_fp8_f32 v191, v48, v50
	v_pk_mul_f32 v[184:185], v[106:107], v[186:187]
	v_med3_f32 v203, v204, s11, v232
	v_med3_f32 v204, v205, s11, v232
	v_cvt_pk_fp8_f32 v189, v203, v204 op_sel:[0,0,1]
	v_lshlrev_b32_e32 v202, 16, v180
	v_and_b32_e32 v203, 0xffff0000, v180
	v_med3_f32 v51, v184, s11, v232
	v_med3_f32 v184, v185, s11, v232
	v_cvt_pk_fp8_f32 v191, v51, v184 op_sel:[0,0,1]
	v_pk_mul_f32 v[50:51], v[56:57], v[202:203]
	v_mov_b32_e32 v194, v49
	v_lshlrev_b32_e32 v180, 16, v181
	v_med3_f32 v48, v50, s11, v232
	v_med3_f32 v50, v51, s11, v232
	v_and_b32_e32 v181, 0xffff0000, v181
	v_cvt_pk_fp8_f32 v194, v48, v50
	v_pk_mul_f32 v[180:181], v[58:59], v[180:181]
	v_lshlrev_b32_e32 v204, 16, v182
	v_and_b32_e32 v205, 0xffff0000, v182
	v_med3_f32 v51, v180, s11, v232
	v_med3_f32 v180, v181, s11, v232
	v_cvt_pk_fp8_f32 v194, v51, v180 op_sel:[0,0,1]
	v_pk_mul_f32 v[50:51], v[52:53], v[204:205]
	v_mov_b32_e32 v195, v49
	v_lshlrev_b32_e32 v182, 16, v183
	v_med3_f32 v48, v50, s11, v232
	v_med3_f32 v50, v51, s11, v232
	v_and_b32_e32 v183, 0xffff0000, v183
	v_cvt_pk_fp8_f32 v195, v48, v50
	v_pk_mul_f32 v[180:181], v[54:55], v[182:183]
	v_lshlrev_b32_e32 v184, 16, v172
	v_and_b32_e32 v185, 0xffff0000, v172
	v_med3_f32 v51, v180, s11, v232
	v_med3_f32 v180, v181, s11, v232
	v_cvt_pk_fp8_f32 v195, v51, v180 op_sel:[0,0,1]
	v_lshlrev_b32_e32 v180, 16, v176
	v_and_b32_e32 v181, 0xffff0000, v176
	v_lshlrev_b32_e32 v186, 16, v173
	v_and_b32_e32 v187, 0xffff0000, v173
	v_pk_mul_f32 v[172:173], v[96:97], v[180:181]
	v_lshlrev_b32_e32 v176, 16, v177
	v_and_b32_e32 v177, 0xffff0000, v177
	v_med3_f32 v48, v172, s11, v232
	v_med3_f32 v173, v173, s11, v232
	v_mov_b32_e32 v172, v49
	v_cvt_pk_fp8_f32 v172, v48, v173
	v_pk_mul_f32 v[176:177], v[98:99], v[176:177]
	v_lshlrev_b32_e32 v182, 16, v178
	v_and_b32_e32 v183, 0xffff0000, v178
	v_med3_f32 v176, v176, s11, v232
	v_med3_f32 v177, v177, s11, v232
	v_cvt_pk_fp8_f32 v172, v176, v177 op_sel:[0,0,1]
	v_pk_mul_f32 v[176:177], v[88:89], v[182:183]
	v_mov_b32_e32 v173, v49
	v_lshlrev_b32_e32 v178, 16, v179
	v_med3_f32 v48, v176, s11, v232
	v_med3_f32 v176, v177, s11, v232
	v_and_b32_e32 v179, 0xffff0000, v179
	v_cvt_pk_fp8_f32 v173, v48, v176
	v_pk_mul_f32 v[178:179], v[90:91], v[178:179]
	v_lshlrev_b64 v[50:51], 10, v[222:223]
	v_lshl_add_u64 v[50:51], s[42:43], 0, v[50:51]
	v_med3_f32 v177, v178, s11, v232
	v_med3_f32 v178, v179, s11, v232
	v_cvt_pk_fp8_f32 v173, v177, v178 op_sel:[0,0,1]
	v_pk_mul_f32 v[176:177], v[44:45], v[184:185]
	v_lshl_add_u64 v[50:51], v[50:51], 0, vcc
	v_lshl_add_u64 v[50:51], v[50:51], 0, s[22:23]
	v_med3_f32 v48, v176, s11, v232
	v_med3_f32 v177, v177, s11, v232
	v_mov_b32_e32 v176, v49
	v_cvt_pk_fp8_f32 v176, v48, v177
	v_pk_mul_f32 v[178:179], v[46:47], v[186:187]
	v_lshl_add_u64 v[50:51], v[50:51], 0, v[216:217]
	v_permlane16_swap_b32_e32 v188, v190
	v_permlane16_swap_b32_e32 v189, v191
	global_store_dwordx4 v[50:51], v[188:191], off
	v_med3_f32 v178, v178, s11, v232
	v_med3_f32 v179, v179, s11, v232
	v_lshlrev_b32_e32 v188, 16, v174
	v_and_b32_e32 v189, 0xffff0000, v174
	v_cvt_pk_fp8_f32 v176, v178, v179 op_sel:[0,0,1]
	v_pk_mul_f32 v[178:179], v[40:41], v[188:189]
	v_mov_b32_e32 v177, v49
	v_lshlrev_b32_e32 v174, 16, v175
	v_med3_f32 v48, v178, s11, v232
	v_med3_f32 v178, v179, s11, v232
	v_and_b32_e32 v175, 0xffff0000, v175
	v_cvt_pk_fp8_f32 v177, v48, v178
	v_pk_mul_f32 v[174:175], v[42:43], v[174:175]
	v_lshlrev_b32_e32 v178, 16, v170
	v_and_b32_e32 v179, 0xffff0000, v170
	v_med3_f32 v174, v174, s11, v232
	v_med3_f32 v175, v175, s11, v232
	v_cvt_pk_fp8_f32 v177, v174, v175 op_sel:[0,0,1]
	v_lshlrev_b32_e32 v174, 16, v168
	v_and_b32_e32 v175, 0xffff0000, v168
	v_pk_mul_f32 v[174:175], v[80:81], v[174:175]
	v_lshlrev_b32_e32 v168, 16, v169
	v_and_b32_e32 v169, 0xffff0000, v169
	v_med3_f32 v48, v174, s11, v232
	v_med3_f32 v175, v175, s11, v232
	v_mov_b32_e32 v174, v49
	v_cvt_pk_fp8_f32 v174, v48, v175
	v_pk_mul_f32 v[168:169], v[82:83], v[168:169]
	v_mov_b32_e32 v175, v49
	v_lshlrev_b32_e32 v170, 16, v171
	v_med3_f32 v168, v168, s11, v232
	v_med3_f32 v169, v169, s11, v232
	v_cvt_pk_fp8_f32 v174, v168, v169 op_sel:[0,0,1]
	v_pk_mul_f32 v[168:169], v[72:73], v[178:179]
	v_and_b32_e32 v171, 0xffff0000, v171
	v_pk_mul_f32 v[170:171], v[74:75], v[170:171]
	v_med3_f32 v48, v168, s11, v232
	v_med3_f32 v168, v169, s11, v232
	v_cvt_pk_fp8_f32 v175, v48, v168
	v_lshlrev_b32_e32 v180, 16, v164
	v_and_b32_e32 v181, 0xffff0000, v164
	v_med3_f32 v169, v170, s11, v232
	v_med3_f32 v170, v171, s11, v232
	v_cvt_pk_fp8_f32 v175, v169, v170 op_sel:[0,0,1]
	v_pk_mul_f32 v[168:169], v[36:37], v[180:181]
	v_mov_b32_e32 v178, v49
	v_lshlrev_b32_e32 v164, 16, v165
	v_med3_f32 v48, v168, s11, v232
	v_med3_f32 v168, v169, s11, v232
	v_and_b32_e32 v165, 0xffff0000, v165
	v_cvt_pk_fp8_f32 v178, v48, v168
	v_pk_mul_f32 v[164:165], v[38:39], v[164:165]
	v_lshlrev_b32_e32 v182, 16, v166
	v_and_b32_e32 v183, 0xffff0000, v166
	v_med3_f32 v164, v164, s11, v232
	v_med3_f32 v165, v165, s11, v232
	v_cvt_pk_fp8_f32 v178, v164, v165 op_sel:[0,0,1]
	v_pk_mul_f32 v[164:165], v[32:33], v[182:183]
	v_mov_b32_e32 v179, v49
	v_lshlrev_b32_e32 v166, 16, v167
	v_med3_f32 v48, v164, s11, v232
	v_med3_f32 v164, v165, s11, v232
	v_and_b32_e32 v167, 0xffff0000, v167
	v_cvt_pk_fp8_f32 v179, v48, v164
	v_pk_mul_f32 v[166:167], v[34:35], v[166:167]
	v_or_b32_e32 v164, 32, v222
	v_permlane16_swap_b32_e32 v172, v174
	v_med3_f32 v165, v166, s11, v232
	v_med3_f32 v166, v167, s11, v232
	v_cvt_pk_fp8_f32 v179, v165, v166 op_sel:[0,0,1]
	v_ashrrev_i32_e32 v165, 31, v164
	v_lshlrev_b64 v[164:165], 10, v[164:165]
	v_lshl_add_u64 v[164:165], s[42:43], 0, v[164:165]
	v_lshl_add_u64 v[164:165], v[164:165], 0, vcc
	v_lshl_add_u64 v[164:165], v[164:165], 0, s[22:23]
	v_lshl_add_u64 v[164:165], v[164:165], 0, v[216:217]
	v_permlane16_swap_b32_e32 v173, v175
	v_permlane16_swap_b32_e32 v176, v178
	v_permlane16_swap_b32_e32 v177, v179
	global_store_dwordx4 v[164:165], v[172:175], off
	global_store_dwordx4 v[164:165], v[176:179], off offset:32
	v_lshlrev_b32_e32 v164, 16, v160
	v_and_b32_e32 v165, 0xffff0000, v160
	v_lshlrev_b32_e32 v168, 16, v156
	v_and_b32_e32 v169, 0xffff0000, v156
	v_lshlrev_b32_e32 v170, 16, v157
	v_and_b32_e32 v171, 0xffff0000, v157
	v_pk_mul_f32 v[156:157], v[28:29], v[164:165]
	v_lshlrev_b32_e32 v160, 16, v161
	v_and_b32_e32 v161, 0xffff0000, v161
	v_med3_f32 v48, v156, s11, v232
	v_med3_f32 v157, v157, s11, v232
	v_mov_b32_e32 v156, v49
	v_cvt_pk_fp8_f32 v156, v48, v157
	v_pk_mul_f32 v[160:161], v[30:31], v[160:161]
	v_lshlrev_b32_e32 v166, 16, v162
	v_and_b32_e32 v167, 0xffff0000, v162
	v_med3_f32 v160, v160, s11, v232
	v_med3_f32 v161, v161, s11, v232
	v_cvt_pk_fp8_f32 v156, v160, v161 op_sel:[0,0,1]
	v_pk_mul_f32 v[160:161], v[24:25], v[166:167]
	v_mov_b32_e32 v157, v49
	v_lshlrev_b32_e32 v162, 16, v163
	v_med3_f32 v48, v160, s11, v232
	v_med3_f32 v160, v161, s11, v232
	v_and_b32_e32 v163, 0xffff0000, v163
	v_cvt_pk_fp8_f32 v157, v48, v160
	v_pk_mul_f32 v[162:163], v[26:27], v[162:163]
	v_lshlrev_b32_e32 v172, 16, v158
	v_and_b32_e32 v173, 0xffff0000, v158
	v_med3_f32 v161, v162, s11, v232
	v_med3_f32 v162, v163, s11, v232
	v_cvt_pk_fp8_f32 v157, v161, v162 op_sel:[0,0,1]
	v_pk_mul_f32 v[160:161], v[68:69], v[168:169]
	v_pk_mul_f32 v[162:163], v[70:71], v[170:171]
	v_med3_f32 v48, v160, s11, v232
	v_med3_f32 v161, v161, s11, v232
	v_mov_b32_e32 v160, v49
	v_cvt_pk_fp8_f32 v160, v48, v161
	v_med3_f32 v162, v162, s11, v232
	v_med3_f32 v163, v163, s11, v232
	v_mov_b32_e32 v161, v49
	v_cvt_pk_fp8_f32 v160, v162, v163 op_sel:[0,0,1]
	v_pk_mul_f32 v[162:163], v[76:77], v[172:173]
	v_lshlrev_b32_e32 v158, 16, v159
	v_and_b32_e32 v159, 0xffff0000, v159
	v_med3_f32 v48, v162, s11, v232
	v_med3_f32 v162, v163, s11, v232
	v_cvt_pk_fp8_f32 v161, v48, v162
	v_pk_mul_f32 v[158:159], v[78:79], v[158:159]
	v_lshlrev_b32_e32 v162, 16, v150
	v_and_b32_e32 v163, 0xffff0000, v150
	v_med3_f32 v158, v158, s11, v232
	v_med3_f32 v159, v159, s11, v232
	v_cvt_pk_fp8_f32 v161, v158, v159 op_sel:[0,0,1]
	v_lshlrev_b32_e32 v158, 16, v148
	v_and_b32_e32 v159, 0xffff0000, v148
	v_pk_mul_f32 v[158:159], v[20:21], v[158:159]
	v_lshlrev_b32_e32 v148, 16, v149
	v_and_b32_e32 v149, 0xffff0000, v149
	v_med3_f32 v48, v158, s11, v232
	v_med3_f32 v159, v159, s11, v232
	v_mov_b32_e32 v158, v49
	v_cvt_pk_fp8_f32 v158, v48, v159
	v_pk_mul_f32 v[148:149], v[22:23], v[148:149]
	v_mov_b32_e32 v159, v49
	v_lshlrev_b32_e32 v150, 16, v151
	v_med3_f32 v148, v148, s11, v232
	v_med3_f32 v149, v149, s11, v232
	v_cvt_pk_fp8_f32 v158, v148, v149 op_sel:[0,0,1]
	v_pk_mul_f32 v[148:149], v[16:17], v[162:163]
	v_and_b32_e32 v151, 0xffff0000, v151
	v_pk_mul_f32 v[150:151], v[18:19], v[150:151]
	v_med3_f32 v48, v148, s11, v232
	v_med3_f32 v148, v149, s11, v232
	v_cvt_pk_fp8_f32 v159, v48, v148
	v_lshlrev_b32_e32 v164, 16, v152
	v_and_b32_e32 v165, 0xffff0000, v152
	v_med3_f32 v149, v150, s11, v232
	v_med3_f32 v150, v151, s11, v232
	v_cvt_pk_fp8_f32 v159, v149, v150 op_sel:[0,0,1]
	v_pk_mul_f32 v[148:149], v[84:85], v[164:165]
	v_mov_b32_e32 v162, v49
	v_lshlrev_b32_e32 v152, 16, v153
	v_med3_f32 v48, v148, s11, v232
	v_med3_f32 v148, v149, s11, v232
	v_and_b32_e32 v153, 0xffff0000, v153
	v_cvt_pk_fp8_f32 v162, v48, v148
	v_pk_mul_f32 v[150:151], v[86:87], v[152:153]
	v_lshlrev_b32_e32 v166, 16, v154
	v_and_b32_e32 v167, 0xffff0000, v154
	v_med3_f32 v149, v150, s11, v232
	v_med3_f32 v150, v151, s11, v232
	v_cvt_pk_fp8_f32 v162, v149, v150 op_sel:[0,0,1]
	v_pk_mul_f32 v[148:149], v[92:93], v[166:167]
	v_mov_b32_e32 v163, v49
	v_lshlrev_b32_e32 v154, 16, v155
	v_med3_f32 v48, v148, s11, v232
	v_med3_f32 v148, v149, s11, v232
	v_and_b32_e32 v155, 0xffff0000, v155
	v_cvt_pk_fp8_f32 v163, v48, v148
	v_pk_mul_f32 v[150:151], v[94:95], v[154:155]
	v_permlane16_swap_b32_e32 v160, v162
	v_permlane16_swap_b32_e32 v156, v158
	v_med3_f32 v149, v150, s11, v232
	v_med3_f32 v150, v151, s11, v232
	v_cvt_pk_fp8_f32 v163, v149, v150 op_sel:[0,0,1]
	v_lshl_add_u64 v[148:149], v[50:51], 0, s[0:1]
	s_mov_b32 s0, 0x20000
	v_add_co_u32_e32 v150, vcc, s0, v50
	v_permlane16_swap_b32_e32 v161, v163
	global_store_dwordx4 v[148:149], v[160:163], off offset:32
	v_lshlrev_b32_e32 v148, 16, v140
	v_and_b32_e32 v149, 0xffff0000, v140
	v_lshlrev_b32_e32 v140, 16, v141
	v_and_b32_e32 v141, 0xffff0000, v141
	v_pk_mul_f32 v[148:149], v[12:13], v[148:149]
	v_pk_mul_f32 v[140:141], v[14:15], v[140:141]
	v_med3_f32 v48, v148, s11, v232
	v_med3_f32 v148, v149, s11, v232
	v_med3_f32 v149, v140, s11, v232
	v_mov_b32_e32 v140, v49
	v_cvt_pk_fp8_f32 v140, v48, v148
	v_permlane16_swap_b32_e32 v157, v159
	v_addc_co_u32_e32 v151, vcc, 0, v51, vcc
	global_store_dwordx4 v[150:151], v[156:159], off
	v_lshlrev_b32_e32 v150, 16, v142
	v_and_b32_e32 v151, 0xffff0000, v142
	v_med3_f32 v141, v141, s11, v232
	v_cvt_pk_fp8_f32 v140, v149, v141 op_sel:[0,0,1]
	v_pk_mul_f32 v[148:149], v[8:9], v[150:151]
	v_mov_b32_e32 v141, v49
	v_lshlrev_b32_e32 v142, 16, v143
	v_med3_f32 v48, v148, s11, v232
	v_med3_f32 v148, v149, s11, v232
	v_and_b32_e32 v143, 0xffff0000, v143
	v_cvt_pk_fp8_f32 v141, v48, v148
	v_pk_mul_f32 v[142:143], v[10:11], v[142:143]
	v_lshlrev_b32_e32 v152, 16, v144
	v_and_b32_e32 v153, 0xffff0000, v144
	v_lshlrev_b32_e32 v144, 16, v145
	v_and_b32_e32 v145, 0xffff0000, v145
	v_med3_f32 v142, v142, s11, v232
	v_med3_f32 v143, v143, s11, v232
	v_cvt_pk_fp8_f32 v141, v142, v143 op_sel:[0,0,1]
	v_pk_mul_f32 v[142:143], v[100:101], v[152:153]
	v_pk_mul_f32 v[144:145], v[102:103], v[144:145]
	v_med3_f32 v48, v142, s11, v232
	v_med3_f32 v142, v143, s11, v232
	v_med3_f32 v143, v144, s11, v232
	v_mov_b32_e32 v144, v49
	v_cvt_pk_fp8_f32 v144, v48, v142
	v_lshlrev_b32_e32 v154, 16, v146
	v_and_b32_e32 v155, 0xffff0000, v146
	v_med3_f32 v145, v145, s11, v232
	v_cvt_pk_fp8_f32 v144, v143, v145 op_sel:[0,0,1]
	v_pk_mul_f32 v[142:143], v[108:109], v[154:155]
	v_mov_b32_e32 v145, v49
	v_lshlrev_b32_e32 v146, 16, v147
	v_med3_f32 v48, v142, s11, v232
	v_med3_f32 v142, v143, s11, v232
	v_and_b32_e32 v147, 0xffff0000, v147
	v_cvt_pk_fp8_f32 v145, v48, v142
	v_pk_mul_f32 v[146:147], v[110:111], v[146:147]
	v_lshlrev_b32_e32 v142, 16, v132
	v_lshlrev_b32_e32 v148, 16, v136
	v_med3_f32 v143, v146, s11, v232
	v_med3_f32 v146, v147, s11, v232
	v_cvt_pk_fp8_f32 v145, v143, v146 op_sel:[0,0,1]
	v_and_b32_e32 v143, 0xffff0000, v132
	v_pk_mul_f32 v[142:143], v[4:5], v[142:143]
	v_lshlrev_b32_e32 v132, 16, v133
	v_and_b32_e32 v133, 0xffff0000, v133
	v_med3_f32 v48, v142, s11, v232
	v_med3_f32 v143, v143, s11, v232
	v_mov_b32_e32 v142, v49
	v_cvt_pk_fp8_f32 v142, v48, v143
	v_pk_mul_f32 v[132:133], v[6:7], v[132:133]
	v_lshlrev_b32_e32 v146, 16, v134
	v_and_b32_e32 v147, 0xffff0000, v134
	v_med3_f32 v132, v132, s11, v232
	v_med3_f32 v133, v133, s11, v232
	v_cvt_pk_fp8_f32 v142, v132, v133 op_sel:[0,0,1]
	v_pk_mul_f32 v[132:133], v[0:1], v[146:147]
	v_mov_b32_e32 v143, v49
	v_lshlrev_b32_e32 v134, 16, v135
	v_med3_f32 v48, v132, s11, v232
	v_med3_f32 v132, v133, s11, v232
	v_and_b32_e32 v135, 0xffff0000, v135
	v_cvt_pk_fp8_f32 v143, v48, v132
	v_pk_mul_f32 v[134:135], v[2:3], v[134:135]
	v_and_b32_e32 v149, 0xffff0000, v136
	v_mov_b32_e32 v146, v49
	v_med3_f32 v133, v134, s11, v232
	v_med3_f32 v134, v135, s11, v232
	v_cvt_pk_fp8_f32 v143, v133, v134 op_sel:[0,0,1]
	v_pk_mul_f32 v[132:133], v[116:117], v[148:149]
	v_lshlrev_b32_e32 v136, 16, v137
	v_and_b32_e32 v137, 0xffff0000, v137
	v_med3_f32 v48, v132, s11, v232
	v_med3_f32 v132, v133, s11, v232
	v_cvt_pk_fp8_f32 v146, v48, v132
	v_pk_mul_f32 v[134:135], v[118:119], v[136:137]
	v_lshlrev_b32_e32 v150, 16, v138
	v_and_b32_e32 v151, 0xffff0000, v138
	v_med3_f32 v133, v134, s11, v232
	v_med3_f32 v134, v135, s11, v232
	v_cvt_pk_fp8_f32 v146, v133, v134 op_sel:[0,0,1]
	v_pk_mul_f32 v[132:133], v[124:125], v[150:151]
	v_mov_b32_e32 v147, v49
	v_lshlrev_b32_e32 v138, 16, v139
	v_med3_f32 v48, v132, s11, v232
	v_med3_f32 v132, v133, s11, v232
	v_and_b32_e32 v139, 0xffff0000, v139
	v_cvt_pk_fp8_f32 v147, v48, v132
	v_pk_mul_f32 v[134:135], v[126:127], v[138:139]
	v_permlane16_swap_b32_e32 v192, v194
	v_permlane16_swap_b32_e32 v193, v195
	v_med3_f32 v133, v134, s11, v232
	v_med3_f32 v134, v135, s11, v232
	v_cvt_pk_fp8_f32 v147, v133, v134 op_sel:[0,0,1]
	s_mov_b64 s[0:1], 0x28000
	global_store_dwordx4 v[50:51], v[192:195], off offset:32
	v_lshl_add_u64 v[132:133], v[50:51], 0, s[0:1]
	v_add_co_u32_e32 v50, vcc, 0x28000, v50
	v_permlane16_swap_b32_e32 v140, v142
	v_permlane16_swap_b32_e32 v141, v143
	v_addc_co_u32_e32 v51, vcc, 0, v51, vcc
	v_permlane16_swap_b32_e32 v144, v146
	v_permlane16_swap_b32_e32 v145, v147
	global_store_dwordx4 v[50:51], v[140:143], off
	global_store_dwordx4 v[132:133], v[144:147], off offset:32
	s_cbranch_execnz .LBB0_444
